# P9 gate-up K-loop: one static s_setprio 1 for the wave half that arrives second (wr==1) instead of per-segment priority toggles, on top of v55
# baseline (speedup 1.0000x reference)
; #define LAS __attribute__((address_space(3)))
; #define G_SRC(i_, R_, C_) do { const int b_ = ltid() * 16 + (i_) * 8192; if (P::FP8) { R_ = b_ >> 7; C_ = (((b_ >> 4) & 7) ^ g8(R_)) << 4; } else { stage_rc(b_, R_, C_); C_ *= 2; } } while (0)
; #define G_GATHER_OFFS(tab_, rv_) do { _Pragma("unroll") for (int i = 0; i < 2; ++i) { int R_, C_; G_SRC(i, R_, C_); const int ra_ = (tab_)[R_], rb_ = (tab_)[HALF + R_];        \
;     vAc[0][i] = (unsigned)((R_ < (rv_) ? ra_ : 0) * KB + C_); vAc[1][i] = (unsigned)((HALF + R_ < (rv_) ? rb_ : 0) * KB + C_); } } while (0)
; #define WAIT_V(n) asm volatile("s_waitcnt vmcnt(" #n ")" ::: "memory")
; #define BAR __builtin_amdgcn_s_barrier()
; template <class P>
; DEV void gemm_stream(const P& pol) {
;     ...
;   for (int i = 0; i < 2; ++i) { int R_, C_; G_SRC(i, R_, C_); const int rho = R_ & 31, Rb = (R_ & ~31) + 8 * ((rho & 15) >> 2) + 4 * (rho >> 4) + (rho & 3); voffB[i] = (unsigned)(Rb * KB + C_); }
;   if (P::GATHER) {
;     pol.arow_fill(cur, (int*)(shm + GEMM_AROW_OFF));
;     __syncthreads();
;     G_GATHER_OFFS(arow, cur.rv);
;   } else {
; #pragma unroll
;     for (int i = 0; i < 2; ++i) { int R_, C_; G_SRC(i, R_, C_); vAc[0][i] = (unsigned)(R_ * KB + C_); vAc[1][i] = vAc[0][i]; }
;   }
;   const size_t kstep = 128, hstep = (size_t)HALF * KB;
;   const unsigned ldsw = (unsigned)wid * 1024u;
;   const int aoff = P::FP8 ? (wr * 64 + fr) * 128 + (((2 * fq) ^ g8(fr)) << 4) : lds_byte(wr * 64 + fr, fq * 8);
;   const int boff = P::FP8 ? (wc * 32 + fr) * 128 + (((2 * fq) ^ g8(fr)) << 4) : lds_byte(wc * 32 + fr, fq * 8);
;   const int aoff1 = (wr * 64 + fr) * 128 + (((2 * fq + 1) ^ g8(fr)) << 4), boff1 = (wc * 32 + fr) * 128 + (((2 * fq + 1) ^ g8(fr)) << 4);
;     ...
;   int sclw = P::SCALE_B, scla = P::SCALE_A;
;   f32x4 acc[2][2][4][2];
;   f32x4 bv[2][2];
;   LAS float* btab = (LAS float*)(shm + GEMM_BIAS_OFF);
;     ...
;   if (P::HASBIAS) { pol.bias_fill(cur, (float*)(shm + GEMM_BIAS_OFF)); __syncthreads(); G_BIAS(btab); G_INIT(); } else G_ZERO();
;   i32x8 At[4], B0[2], B1[2];
;   int rvw = P::ROWSKIP ? cur.rv - 64 * wr : 256;
;   const char* cA0 = pol.abase(cur, 0); const char* cA1 = pol.abase(cur, 1); const char* cB = pol.bbase(cur);
;   G_STAGE(G_SB(0, 0), cB, voffB); G_STAGE(G_SA(0, 0), cA0, vAc[0]); G_STAGE(G_SB(0, 1), cB + hstep, voffB); G_STAGE(G_SA(0, 1), cA1, vAc[1]);
;   if (wr == 1) BAR;
;   WAIT_V(4); BAR;
.LBB0_1440:
	s_or_b64 exec, exec, s[12:13]
	v_bfe_u32 v14, v12, 1, 3
	v_add_u32_e32 v14, 2, v14
	v_lshlrev_b32_e32 v15, 1, v14
	v_and_b32_e32 v15, 6, v15
	v_bfe_i32 v14, v14, 2, 1
	v_add3_u32 v14, v14, v15, 1
	v_bitop3_b32 v13, v14, v13, 7 bitop3:0x78
	s_waitcnt lgkmcnt(0)
	v_lshlrev_b32_e32 v4, 11, v4
	v_cmp_gt_i32_e32 vcc, s14, v12
	v_lshlrev_b32_e32 v13, 4, v13
	v_add_u32_e32 v14, 0x80, v12
	v_cndmask_b32_e32 v4, 0, v4, vcc
	v_add_u32_e32 v178, v13, v4
	v_lshlrev_b32_e32 v4, 11, v5
	v_cmp_gt_i32_e32 vcc, s14, v14
	v_lshlrev_b32_e32 v2, 11, v2
	v_mov_b32_e32 v191, 0x2000
	v_cndmask_b32_e32 v4, 0, v4, vcc
	v_add_u32_e32 v186, v13, v4
	v_bfe_u32 v4, v10, 1, 3
	v_add_u32_e32 v4, 2, v4
	v_lshlrev_b32_e32 v5, 1, v4
	v_and_b32_e32 v5, 6, v5
	v_bfe_i32 v4, v4, 2, 1
	v_add3_u32 v4, v4, v5, 1
	v_bitop3_b32 v4, v4, v11, 7 bitop3:0x78
	v_cmp_gt_i32_e32 vcc, s14, v10
	v_lshlrev_b32_e32 v4, 4, v4
	v_add_u32_e32 v5, 0x80, v10
	v_cndmask_b32_e32 v2, 0, v2, vcc
	v_add_u32_e32 v184, v4, v2
	v_lshlrev_b32_e32 v2, 11, v3
	v_cmp_gt_i32_e32 vcc, s14, v5
	s_ashr_i32 s6, s54, 6
	s_and_b32 s19, s6, 3
	v_cndmask_b32_e32 v2, 0, v2, vcc
	v_add_u32_e32 v188, v4, v2
	v_ashrrev_i32_e32 v2, 3, v9
	v_bfe_u32 v3, v2, 1, 3
	v_add_u32_e32 v3, 2, v3
	v_lshlrev_b32_e32 v4, 1, v3
	v_and_b32_e32 v4, 6, v4
	v_bfe_i32 v3, v3, 2, 1
	v_add3_u32 v3, v3, v4, 1
	v_lshlrev_b32_e32 v4, 1, v2
	v_lshrrev_b32_e32 v5, 2, v2
	v_and_b32_e32 v4, 24, v4
	v_and_b32_e32 v5, 4, v5
	v_and_b32_e32 v2, 0x1fffe3, v2
	v_or3_b32 v2, v2, v4, v5
	v_bitop3_b32 v3, v3, v9, 7 bitop3:0x78
	v_lshlrev_b32_e32 v2, 11, v2
	v_lshl_add_u32 v180, v3, 4, v2
	v_lshl_add_u32 v2, v8, 4, v191
	v_ashrrev_i32_e32 v2, 7, v2
	v_bfe_u32 v3, v2, 1, 3
	v_add_u32_e32 v3, 2, v3
	v_lshlrev_b32_e32 v4, 1, v3
	v_and_b32_e32 v4, 6, v4
	v_bfe_i32 v3, v3, 2, 1
	v_add3_u32 v3, v3, v4, 1
	v_lshlrev_b32_e32 v4, 1, v2
	v_lshrrev_b32_e32 v5, 2, v2
	v_and_b32_e32 v4, 24, v4
	v_and_b32_e32 v5, 4, v5
	v_and_b32_e32 v2, 0x1fffe3, v2
	s_lshl_b32 s12, s6, 10
	v_or3_b32 v2, v2, v4, v5
	s_lshl_b32 s6, s19, 7
	s_waitcnt vmcnt(3)
	v_bfe_u32 v20, v1, 4, 2
	v_bitop3_b32 v3, v3, v8, 7 bitop3:0x78
	v_lshlrev_b32_e32 v2, 11, v2
	s_add_i32 s6, s6, 0
	v_lshl_add_u32 v182, v3, 4, v2
	v_lshl_add_u32 v2, v20, 5, s6
	s_lshl_b32 s6, s18, 8
	s_ashr_i32 s7, s6, 31
	v_lshlrev_b64 v[6:7], 23, v[6:7]
	s_lshl_b64 s[6:7], s[6:7], 11
	v_lshl_add_u64 v[6:7], s[4:5], 0, v[6:7]
	s_add_i32 s58, s12, 0
	v_mov_b32_e32 v179, 0
	v_lshl_add_u64 v[10:11], v[6:7], 0, s[6:7]
	s_add_i32 s59, s58, 0x10000
	v_mov_b32_e32 v181, v179
	v_add_u32_e32 v202, 0x25d90, v2
	v_lshl_add_u64 v[12:13], v[10:11], 0, v[180:181]
	s_mov_b32 m0, s59
	v_mov_b32_e32 v183, v179
	s_add_i32 s60, s58, 0x12000
	s_barrier
	ds_read_b128 v[50:53], v202 offset:16
	ds_read_b128 v[2:5], v202 offset:528
	global_load_lds_dwordx4 v[12:13], off
	v_lshl_add_u64 v[14:15], v[10:11], 0, v[182:183]
	s_mov_b32 m0, s60
	s_add_i32 s61, s58, 0x2000
	global_load_lds_dwordx4 v[14:15], off
	s_mov_b32 m0, s58
	s_mov_b64 s[12:13], 0x40000
	global_load_lds_dwordx4 v178, s[10:11]
	s_mov_b32 m0, s61
	v_lshl_add_u64 v[6:7], v[10:11], 0, s[12:13]
	s_add_i32 s62, s58, 0x14000
	global_load_lds_dwordx4 v184, s[10:11]
	v_lshl_add_u64 v[8:9], v[6:7], 0, v[180:181]
	s_mov_b32 m0, s62
	s_add_i32 s63, s58, 0x16000
	global_load_lds_dwordx4 v[8:9], off
	v_lshl_add_u64 v[6:7], v[6:7], 0, v[182:183]
	s_mov_b32 m0, s63
	s_add_i32 s64, s58, 0x4000
	global_load_lds_dwordx4 v[6:7], off
	s_mov_b32 m0, s64
	s_add_i32 s65, s58, 0x6000
	global_load_lds_dwordx4 v186, s[10:11]
	s_mov_b32 m0, s65
	s_ashr_i32 s20, s54, 8
	global_load_lds_dwordx4 v188, s[10:11]
	ds_read_b128 v[54:57], v202
	ds_read_b128 v[6:9], v202 offset:512
	s_lshl_b32 s21, s19, 5
	v_mov_b32_e32 v185, v179
	s_movk_i32 s66, 0x80
	s_mov_b32 s67, 0
	v_lshl_add_u64 v[18:19], s[10:11], 0, v[178:179]
	s_cmp_lg_u32 s20, 1
	v_lshl_add_u64 v[16:17], s[10:11], 0, v[184:185]
	s_cbranch_scc1 .LBB0_1442
	s_setprio 1
	s_barrier

; #define LAS __attribute__((address_space(3)))
; #define G_GATHER_OFFS(tab_, rv_) do { _Pragma("unroll") for (int i = 0; i < 2; ++i) { int R_, C_; G_SRC(i, R_, C_); const int ra_ = (tab_)[R_], rb_ = (tab_)[HALF + R_];        \
;     vAc[0][i] = (unsigned)((R_ < (rv_) ? ra_ : 0) * KB + C_); vAc[1][i] = (unsigned)((HALF + R_ < (rv_) ? rb_ : 0) * KB + C_); } } while (0)
; #define G_STAGE(bufoff, gbase, voff) do { _Pragma("unroll") for (int _i = 0; _i < 2; ++_i) \
;     __builtin_amdgcn_global_load_lds((const unsigned*)((const char*)(gbase) + (voff)[_i]), (LAS unsigned*)(lds + (bufoff) + ldsw + _i * 8192), 16, 0, 0); } while (0)
; #define G_LDA(dst, b, h) do { _Pragma("unroll") for (int m = 0; m < 4; ++m) dst[m] = G_LD2(G_SA(b, h) + aoff + m * 2048, G_SA(b, h) + (P::FP8 ? aoff1 : aoff + 1024) + m * 2048); } while (0)
; #define G_LDB(dst, b, h) do { _Pragma("unroll") for (int n = 0; n < 2; ++n) dst[n] = G_LD2(G_SB(b, h) + boff + n * 2048, G_SB(b, h) + (P::FP8 ? boff1 : boff + 1024) + n * 2048); } while (0)
; #define WAIT_V(n) asm volatile("s_waitcnt vmcnt(" #n ")" ::: "memory")
; #define WAIT_L(n) asm volatile("s_waitcnt lgkmcnt(" #n ")" ::: "memory")
; #define BAR __builtin_amdgcn_s_barrier()
; template <class P>
; DEV void gemm_stream(const P& pol) {
;     ...
;   for (;;) {
;     const bool has_next = pol.get(ui + 1, nxt);
;     const char* nA0 = has_next ? pol.abase(nxt, 0) : cA0; const char* nA1 = has_next ? pol.abase(nxt, 1) : cA1; const char* nB = has_next ? pol.bbase(nxt) : cB;
;     for (int t = 0; t < nt; t += 2) {
;       const bool last = (t == nt - 2);
;       const size_t k1 = (size_t)(t + 1) * kstep, k2 = (size_t)(t + 2) * kstep;
;       const char* a20 = last ? nA0 : cA0 + k2; const char* a21 = last ? nA1 : cA1 + k2; const char* b2 = last ? nB : cB + k2;
;       G_LDB(B0, 0, 0); SCHED; G_LDA(At, 0, 0); G_STAGE(G_SA(1, 1), cA1 + k1, vAc[1]);
;       WAIT_L(8); BAR; WAIT_L(0); G_MMA(0, 0, At, B0); BAR; SCHED;
;       if (P::GATHER && last && has_next) { LAS int* tab = arow + ((ui + 1) & 1) * 256; G_GATHER_OFFS(tab, nxt.rv); }
;       G_LDB(B1, 0, 1); G_STAGE(G_SB(0, 0), b2, voffB);
;       BAR; WAIT_L(0); G_MMA(0, 1, At, B1); BAR;
;       G_LDA(At, 0, 1); G_STAGE(G_SA(0, 0), a20, vAc[0]);
;       BAR; WAIT_L(0); G_MMA(1, 0, At, B0); BAR; SCHED;
;       G_STAGE(G_SB(0, 1), b2 + hstep, voffB);
;       WAIT_V(6); BAR; G_MMA(1, 1, At, B1); BAR;
.LBB0_1446:
	ds_read_b128 v[14:17], v209
	ds_read_b128 v[18:21], v205
	ds_read_b128 v[22:25], v210
	ds_read_b128 v[26:29], v211
	s_lshl_b32 s6, s67, 8
	s_waitcnt lgkmcnt(0)
	v_pk_add_f32 v[64:65], v[8:9], 1.0 op_sel_hi:[1,0]
	v_pk_add_f32 v[62:63], v[6:7], 1.0 op_sel_hi:[1,0]
	v_pk_add_f32 v[60:61], v[4:5], 1.0 op_sel_hi:[1,0]
	v_pk_add_f32 v[58:59], v[2:3], 1.0 op_sel_hi:[1,0]
	s_ashr_i32 s37, s36, 31
	s_and_b32 s93, s6, 0x100
	v_mov_b32_e32 v187, v179
	v_lshl_add_u64 v[2:3], s[10:11], 0, v[186:187]
	s_mov_b32 m0, s85
	v_lshl_add_u64 v[4:5], v[2:3], 0, s[14:15]
	v_mov_b32_e32 v189, v179
	v_add_u32_e32 v227, v204, v203
	ds_read_b128 v[30:33], v221
	ds_read_b128 v[38:41], v221 offset:2048
	ds_read_b128 v[34:37], v227
	ds_read_b128 v[42:45], v227 offset:2048
	ds_read_b128 v[66:69], v221 offset:4096
	ds_read_b128 v[74:77], v221 offset:6144
	ds_read_b128 v[70:73], v227 offset:4096
	ds_read_b128 v[78:81], v227 offset:6144
	global_load_lds_dwordx4 v[4:5], off
	v_lshl_add_u64 v[4:5], s[10:11], 0, v[188:189]
	v_lshl_add_u64 v[6:7], v[4:5], 0, s[14:15]
	s_mov_b32 m0, s86
	s_nop 0
	global_load_lds_dwordx4 v[6:7], off
	s_waitcnt lgkmcnt(8)
	s_barrier
	s_waitcnt lgkmcnt(0)
	v_mov_b64_e32 v[172:173], v[56:57]
	v_mov_b64_e32 v[164:165], v[52:53]
	v_mov_b64_e32 v[156:157], v[56:57]
	v_mov_b64_e32 v[148:149], v[52:53]
	v_mov_b64_e32 v[140:141], v[56:57]
	v_mov_b64_e32 v[132:133], v[52:53]
	v_mov_b64_e32 v[124:125], v[56:57]
	v_mov_b64_e32 v[108:109], v[52:53]
	v_mov_b64_e32 v[170:171], v[54:55]
	v_mov_b64_e32 v[162:163], v[50:51]
	v_mov_b64_e32 v[154:155], v[54:55]
	v_mov_b64_e32 v[146:147], v[50:51]
	v_mov_b64_e32 v[138:139], v[54:55]
	v_mov_b64_e32 v[130:131], v[50:51]
	v_mov_b64_e32 v[122:123], v[54:55]
	v_mov_b64_e32 v[106:107], v[50:51]
	s_waitcnt lgkmcnt(0)
	v_mfma_scale_f32_16x16x128_f8f6f4 v[170:173], v[14:21], v[30:37], v[170:173], v222, v224 op_sel_hi:[0,0,0]
	v_mfma_scale_f32_16x16x128_f8f6f4 v[162:165], v[22:29], v[30:37], v[162:165], v222, v224 op_sel_hi:[0,0,0]
	v_mfma_scale_f32_16x16x128_f8f6f4 v[154:157], v[14:21], v[38:45], v[154:157], v222, v224 op_sel_hi:[0,0,0]
	v_mfma_scale_f32_16x16x128_f8f6f4 v[146:149], v[22:29], v[38:45], v[146:149], v222, v224 op_sel_hi:[0,0,0]
	v_mfma_scale_f32_16x16x128_f8f6f4 v[138:141], v[14:21], v[66:73], v[138:141], v222, v224 op_sel_hi:[0,0,0]
	v_mfma_scale_f32_16x16x128_f8f6f4 v[130:133], v[22:29], v[66:73], v[130:133], v222, v224 op_sel_hi:[0,0,0]
	v_mfma_scale_f32_16x16x128_f8f6f4 v[122:125], v[14:21], v[74:81], v[122:125], v222, v224 op_sel_hi:[0,0,0]
	v_mfma_scale_f32_16x16x128_f8f6f4 v[106:109], v[22:29], v[74:81], v[106:109], v222, v224 op_sel_hi:[0,0,0]
	s_barrier
	v_lshl_add_u64 v[6:7], v[10:11], 0, v[180:181]
	s_mov_b32 m0, s59
	v_lshl_add_u64 v[8:9], v[6:7], 0, s[24:25]
	ds_read_b128 v[192:195], v212
	ds_read_b128 v[196:199], v206
	ds_read_b128 v[228:231], v213
	ds_read_b128 v[232:235], v214
	global_load_lds_dwordx4 v[8:9], off
	v_lshl_add_u64 v[8:9], v[10:11], 0, v[182:183]
	v_lshl_add_u64 v[12:13], v[8:9], 0, s[24:25]
	s_mov_b32 m0, s60
	s_nop 0
	global_load_lds_dwordx4 v[12:13], off
	s_barrier
	s_waitcnt lgkmcnt(0)
	v_mov_b64_e32 v[176:177], v[64:65]
	v_mov_b64_e32 v[168:169], v[60:61]
	v_mov_b64_e32 v[160:161], v[64:65]
	v_mov_b64_e32 v[152:153], v[60:61]
	v_mov_b64_e32 v[144:145], v[64:65]
	v_mov_b64_e32 v[136:137], v[60:61]
	v_mov_b64_e32 v[128:129], v[64:65]
	v_mov_b64_e32 v[120:121], v[60:61]
	v_mov_b64_e32 v[174:175], v[62:63]
	v_mov_b64_e32 v[166:167], v[58:59]
	v_mov_b64_e32 v[158:159], v[62:63]
	v_mov_b64_e32 v[150:151], v[58:59]
	v_mov_b64_e32 v[142:143], v[62:63]
	v_mov_b64_e32 v[134:135], v[58:59]
	v_mov_b64_e32 v[126:127], v[62:63]
	v_mov_b64_e32 v[118:119], v[58:59]
	s_waitcnt lgkmcnt(0)
	v_mfma_scale_f32_16x16x128_f8f6f4 v[174:177], v[192:199], v[30:37], v[174:177], v222, v224 op_sel_hi:[0,0,0]
	v_mfma_scale_f32_16x16x128_f8f6f4 v[166:169], v[228:235], v[30:37], v[166:169], v222, v224 op_sel_hi:[0,0,0]
	v_mfma_scale_f32_16x16x128_f8f6f4 v[158:161], v[192:199], v[38:45], v[158:161], v222, v224 op_sel_hi:[0,0,0]
	v_mfma_scale_f32_16x16x128_f8f6f4 v[150:153], v[228:235], v[38:45], v[150:153], v222, v224 op_sel_hi:[0,0,0]
	v_mfma_scale_f32_16x16x128_f8f6f4 v[142:145], v[192:199], v[66:73], v[142:145], v222, v224 op_sel_hi:[0,0,0]
	v_mfma_scale_f32_16x16x128_f8f6f4 v[134:137], v[228:235], v[66:73], v[134:137], v222, v224 op_sel_hi:[0,0,0]
	v_mfma_scale_f32_16x16x128_f8f6f4 v[126:129], v[192:199], v[74:81], v[126:129], v222, v224 op_sel_hi:[0,0,0]
	v_mfma_scale_f32_16x16x128_f8f6f4 v[118:121], v[228:235], v[74:81], v[118:121], v222, v224 op_sel_hi:[0,0,0]
	v_lshl_add_u64 v[12:13], s[10:11], 0, v[178:179]
	s_mov_b32 m0, s58
	v_lshl_add_u64 v[46:47], v[12:13], 0, s[24:25]
	v_mov_b32_e32 v185, v179
	s_barrier
	ds_read_b128 v[30:33], v221 offset:16384
	ds_read_b128 v[38:41], v221 offset:18432
	ds_read_b128 v[34:37], v227 offset:16384
	ds_read_b128 v[42:45], v227 offset:18432
	ds_read_b128 v[236:239], v221 offset:20480
	ds_read_b128 v[244:247], v221 offset:22528
	ds_read_b128 v[240:243], v227 offset:20480
	ds_read_b128 v[248:251], v227 offset:22528
	global_load_lds_dwordx4 v[46:47], off
	v_lshl_add_u64 v[46:47], s[10:11], 0, v[184:185]
	v_lshl_add_u64 v[48:49], v[46:47], 0, s[24:25]
	s_mov_b32 m0, s61
	s_nop 0
	global_load_lds_dwordx4 v[48:49], off
	s_barrier
; #define LAS __attribute__((address_space(3)))
; #define G_GATHER_OFFS(tab_, rv_) do { _Pragma("unroll") for (int i = 0; i < 2; ++i) { int R_, C_; G_SRC(i, R_, C_); const int ra_ = (tab_)[R_], rb_ = (tab_)[HALF + R_];        \
;     vAc[0][i] = (unsigned)((R_ < (rv_) ? ra_ : 0) * KB + C_); vAc[1][i] = (unsigned)((HALF + R_ < (rv_) ? rb_ : 0) * KB + C_); } } while (0)
; #define G_STAGE(bufoff, gbase, voff) do { _Pragma("unroll") for (int _i = 0; _i < 2; ++_i) \
;     __builtin_amdgcn_global_load_lds((const unsigned*)((const char*)(gbase) + (voff)[_i]), (LAS unsigned*)(lds + (bufoff) + ldsw + _i * 8192), 16, 0, 0); } while (0)
; #define G_LDA(dst, b, h) do { _Pragma("unroll") for (int m = 0; m < 4; ++m) dst[m] = G_LD2(G_SA(b, h) + aoff + m * 2048, G_SA(b, h) + (P::FP8 ? aoff1 : aoff + 1024) + m * 2048); } while (0)
; #define G_LDB(dst, b, h) do { _Pragma("unroll") for (int n = 0; n < 2; ++n) dst[n] = G_LD2(G_SB(b, h) + boff + n * 2048, G_SB(b, h) + (P::FP8 ? boff1 : boff + 1024) + n * 2048); } while (0)
; #define WAIT_V(n) asm volatile("s_waitcnt vmcnt(" #n ")" ::: "memory")
; #define WAIT_L(n) asm volatile("s_waitcnt lgkmcnt(" #n ")" ::: "memory")
; #define BAR __builtin_amdgcn_s_barrier()
; #define SCHED __builtin_amdgcn_sched_barrier(0)
; template <class P>
; DEV void gemm_stream(const P& pol) {
;     ...
;       G_LDB(B0, 0, 0); SCHED; G_LDA(At, 0, 0); G_STAGE(G_SA(1, 1), cA1 + k1, vAc[1]);
;       WAIT_L(8); BAR; WAIT_L(0); G_MMA(0, 0, At, B0); BAR; SCHED;
;       if (P::GATHER && last && has_next) { LAS int* tab = arow + ((ui + 1) & 1) * 256; G_GATHER_OFFS(tab, nxt.rv); }
;       G_LDB(B1, 0, 1); G_STAGE(G_SB(0, 0), b2, voffB);
;       BAR; WAIT_L(0); G_MMA(0, 1, At, B1); BAR;
;       G_LDA(At, 0, 1); G_STAGE(G_SA(0, 0), a20, vAc[0]);
;       BAR; WAIT_L(0); G_MMA(1, 0, At, B0); BAR; SCHED;
;       G_STAGE(G_SB(0, 1), b2 + hstep, voffB);
;       WAIT_V(6); BAR; G_MMA(1, 1, At, B1); BAR;
;       G_LDB(B0, 1, 0); SCHED; G_LDA(At, 1, 0); G_STAGE(G_SA(0, 1), a21, vAc[1]);
;       WAIT_L(8); BAR; WAIT_L(0); G_MMA(0, 0, At, B0); BAR; SCHED;
	s_waitcnt lgkmcnt(0)
	v_mov_b64_e32 v[112:113], v[56:57]
	v_mov_b64_e32 v[100:101], v[52:53]
	v_mov_b64_e32 v[92:93], v[56:57]
	v_mov_b64_e32 v[84:85], v[52:53]
	v_mov_b64_e32 v[76:77], v[56:57]
	v_mov_b64_e32 v[68:69], v[52:53]
	v_mov_b64_e32 v[110:111], v[54:55]
	v_mov_b64_e32 v[98:99], v[50:51]
	v_mov_b64_e32 v[90:91], v[54:55]
	v_mov_b64_e32 v[82:83], v[50:51]
	v_mov_b64_e32 v[74:75], v[54:55]
	v_mov_b64_e32 v[66:67], v[50:51]
	s_waitcnt lgkmcnt(0)
	v_mfma_scale_f32_16x16x128_f8f6f4 v[110:113], v[14:21], v[30:37], v[110:113], v222, v224 op_sel_hi:[0,0,0]
	v_mfma_scale_f32_16x16x128_f8f6f4 v[98:101], v[22:29], v[30:37], v[98:101], v222, v224 op_sel_hi:[0,0,0]
	v_mfma_scale_f32_16x16x128_f8f6f4 v[90:93], v[14:21], v[38:45], v[90:93], v222, v224 op_sel_hi:[0,0,0]
	v_mfma_scale_f32_16x16x128_f8f6f4 v[82:85], v[22:29], v[38:45], v[82:85], v222, v224 op_sel_hi:[0,0,0]
	v_mfma_scale_f32_16x16x128_f8f6f4 v[74:77], v[14:21], v[236:243], v[74:77], v222, v224 op_sel_hi:[0,0,0]
	v_mfma_scale_f32_16x16x128_f8f6f4 v[66:69], v[22:29], v[236:243], v[66:69], v222, v224 op_sel_hi:[0,0,0]
	v_mfma_scale_f32_16x16x128_f8f6f4 v[54:57], v[14:21], v[244:251], v[54:57], v222, v224 op_sel_hi:[0,0,0]
	v_mfma_scale_f32_16x16x128_f8f6f4 v[50:53], v[22:29], v[244:251], v[50:53], v222, v224 op_sel_hi:[0,0,0]
	s_barrier
	v_lshl_add_u64 v[14:15], v[10:11], 0, s[26:27]
	s_mov_b32 m0, s62
	v_lshl_add_u64 v[16:17], v[14:15], 0, v[180:181]
	global_load_lds_dwordx4 v[16:17], off
	v_lshl_add_u64 v[14:15], v[14:15], 0, v[182:183]
	s_mov_b32 m0, s63
	s_nop 0
	global_load_lds_dwordx4 v[14:15], off
	s_waitcnt vmcnt(6)
	s_barrier
	v_mov_b64_e32 v[116:117], v[64:65]
	v_mov_b64_e32 v[104:105], v[60:61]
	v_mov_b64_e32 v[96:97], v[64:65]
	v_mov_b64_e32 v[88:89], v[60:61]
	v_mov_b64_e32 v[80:81], v[64:65]
	v_mov_b64_e32 v[72:73], v[60:61]
	v_mov_b64_e32 v[114:115], v[62:63]
	v_mov_b64_e32 v[102:103], v[58:59]
	v_mov_b64_e32 v[94:95], v[62:63]
	v_mov_b64_e32 v[86:87], v[58:59]
	v_mov_b64_e32 v[78:79], v[62:63]
	v_mov_b64_e32 v[70:71], v[58:59]
	v_mfma_scale_f32_16x16x128_f8f6f4 v[114:117], v[192:199], v[30:37], v[114:117], v222, v224 op_sel_hi:[0,0,0]
	v_mfma_scale_f32_16x16x128_f8f6f4 v[102:105], v[228:235], v[30:37], v[102:105], v222, v224 op_sel_hi:[0,0,0]
	v_mfma_scale_f32_16x16x128_f8f6f4 v[94:97], v[192:199], v[38:45], v[94:97], v222, v224 op_sel_hi:[0,0,0]
	v_mfma_scale_f32_16x16x128_f8f6f4 v[86:89], v[228:235], v[38:45], v[86:89], v222, v224 op_sel_hi:[0,0,0]
	v_mfma_scale_f32_16x16x128_f8f6f4 v[78:81], v[192:199], v[236:243], v[78:81], v222, v224 op_sel_hi:[0,0,0]
	v_mfma_scale_f32_16x16x128_f8f6f4 v[70:73], v[228:235], v[236:243], v[70:73], v222, v224 op_sel_hi:[0,0,0]
	v_mfma_scale_f32_16x16x128_f8f6f4 v[62:65], v[192:199], v[244:251], v[62:65], v222, v224 op_sel_hi:[0,0,0]
	v_mfma_scale_f32_16x16x128_f8f6f4 v[58:61], v[228:235], v[244:251], v[58:61], v222, v224 op_sel_hi:[0,0,0]
	s_barrier
	ds_read_b128 v[14:17], v215
	ds_read_b128 v[18:21], v207
	ds_read_b128 v[22:25], v216
	ds_read_b128 v[26:29], v217
	s_mov_b32 m0, s64
	v_lshl_add_u64 v[2:3], v[2:3], 0, s[24:25]
	ds_read_b128 v[30:33], v221 offset:32768
	ds_read_b128 v[38:41], v221 offset:34816
	ds_read_b128 v[34:37], v227 offset:32768
	ds_read_b128 v[42:45], v227 offset:34816
	ds_read_b128 v[192:195], v221 offset:36864
	ds_read_b128 v[228:231], v221 offset:38912
	ds_read_b128 v[196:199], v227 offset:36864
	ds_read_b128 v[232:235], v227 offset:38912
	global_load_lds_dwordx4 v[2:3], off
	v_lshl_add_u64 v[2:3], v[4:5], 0, s[24:25]
	s_mov_b32 m0, s65
	s_nop 0
	global_load_lds_dwordx4 v[2:3], off
	s_waitcnt lgkmcnt(8)
	s_barrier
	s_waitcnt lgkmcnt(0)
	s_waitcnt lgkmcnt(0)
	v_mfma_scale_f32_16x16x128_f8f6f4 v[170:173], v[14:21], v[30:37], v[170:173], v222, v224 op_sel_hi:[0,0,0]
	v_mfma_scale_f32_16x16x128_f8f6f4 v[162:165], v[22:29], v[30:37], v[162:165], v222, v224 op_sel_hi:[0,0,0]
	v_mfma_scale_f32_16x16x128_f8f6f4 v[154:157], v[14:21], v[38:45], v[154:157], v222, v224 op_sel_hi:[0,0,0]
	v_mfma_scale_f32_16x16x128_f8f6f4 v[146:149], v[22:29], v[38:45], v[146:149], v222, v224 op_sel_hi:[0,0,0]
	v_mfma_scale_f32_16x16x128_f8f6f4 v[138:141], v[14:21], v[192:199], v[138:141], v222, v224 op_sel_hi:[0,0,0]
	v_mfma_scale_f32_16x16x128_f8f6f4 v[130:133], v[22:29], v[192:199], v[130:133], v222, v224 op_sel_hi:[0,0,0]
	v_mfma_scale_f32_16x16x128_f8f6f4 v[122:125], v[14:21], v[228:235], v[122:125], v222, v224 op_sel_hi:[0,0,0]
	v_mfma_scale_f32_16x16x128_f8f6f4 v[106:109], v[22:29], v[228:235], v[106:109], v222, v224 op_sel_hi:[0,0,0]
	s_barrier
; #define G_STAGE(bufoff, gbase, voff) do { _Pragma("unroll") for (int _i = 0; _i < 2; ++_i) \
;     __builtin_amdgcn_global_load_lds((const unsigned*)((const char*)(gbase) + (voff)[_i]), (LAS unsigned*)(lds + (bufoff) + ldsw + _i * 8192), 16, 0, 0); } while (0)
; #define G_LDA(dst, b, h) do { _Pragma("unroll") for (int m = 0; m < 4; ++m) dst[m] = G_LD2(G_SA(b, h) + aoff + m * 2048, G_SA(b, h) + (P::FP8 ? aoff1 : aoff + 1024) + m * 2048); } while (0)
; #define G_LDB(dst, b, h) do { _Pragma("unroll") for (int n = 0; n < 2; ++n) dst[n] = G_LD2(G_SB(b, h) + boff + n * 2048, G_SB(b, h) + (P::FP8 ? boff1 : boff + 1024) + n * 2048); } while (0)
; #define WAIT_V(n) asm volatile("s_waitcnt vmcnt(" #n ")" ::: "memory")
; #define WAIT_L(n) asm volatile("s_waitcnt lgkmcnt(" #n ")" ::: "memory")
; #define BAR __builtin_amdgcn_s_barrier()
; #define SCHED __builtin_amdgcn_sched_barrier(0)
;   DEV void bias_dma(const Unit& u, LAS float* tabw) const { __builtin_amdgcn_global_load_lds((const unsigned*)bias_src(u, ltid() & 255), (LAS unsigned*)tabw, 4, 0, 0); }
;   DEV void bias_dma(const Unit& u, LAS float* tabw) const { __builtin_amdgcn_global_load_lds((const unsigned*)bias_src(u, ltid() & 255), (LAS unsigned*)tabw, 4, 0, 0); }
; template <class P>
; DEV void gemm_stream(const P& pol) {
;     ...
;       WAIT_V(6); BAR; G_MMA(1, 1, At, B1); BAR;
;       G_LDB(B0, 1, 0); SCHED; G_LDA(At, 1, 0); G_STAGE(G_SA(0, 1), a21, vAc[1]);
;       WAIT_L(8); BAR; WAIT_L(0); G_MMA(0, 0, At, B0); BAR; SCHED;
;       G_LDB(B1, 1, 1); G_STAGE(G_SB(1, 0), b2 + kstep, voffB);
;       BAR; WAIT_L(0); G_MMA(0, 1, At, B1); BAR;
;       G_LDA(At, 1, 1); G_STAGE(G_SA(1, 0), a20 + kstep, vAc[0]);
;       BAR; WAIT_L(0); G_MMA(1, 0, At, B0); BAR; SCHED;
;       G_STAGE(G_SB(1, 1), b2 + hstep + kstep, voffB);
;       WAIT_V(6); BAR; G_MMA(1, 1, At, B1); BAR;
;       if (P::HASBIAS && has_next && t == 0) pol.bias_dma(nxt, btab + ((ui + 1) & 1) * 256 + ((wid & 3) << 6));
;       if (P::GATHER && has_next && t == 0) pol.arow_dma(nxt, arow + ((ui + 1) & 1) * 256 + ((wid & 3) << 6));
	s_mov_b32 m0, s68
	v_lshl_add_u64 v[2:3], v[6:7], 0, s[22:23]
	ds_read_b128 v[236:239], v218
	ds_read_b128 v[240:243], v208
	ds_read_b128 v[244:247], v219
	ds_read_b128 v[248:251], v220
	global_load_lds_dwordx4 v[2:3], off
	v_lshl_add_u64 v[2:3], v[8:9], 0, s[22:23]
	s_mov_b32 m0, s69
	s_nop 0
	global_load_lds_dwordx4 v[2:3], off
	s_barrier
	s_waitcnt lgkmcnt(0)
	s_waitcnt lgkmcnt(0)
	v_mfma_scale_f32_16x16x128_f8f6f4 v[174:177], v[236:243], v[30:37], v[174:177], v222, v224 op_sel_hi:[0,0,0]
	v_mfma_scale_f32_16x16x128_f8f6f4 v[166:169], v[244:251], v[30:37], v[166:169], v222, v224 op_sel_hi:[0,0,0]
	v_mfma_scale_f32_16x16x128_f8f6f4 v[158:161], v[236:243], v[38:45], v[158:161], v222, v224 op_sel_hi:[0,0,0]
	v_mfma_scale_f32_16x16x128_f8f6f4 v[150:153], v[244:251], v[38:45], v[150:153], v222, v224 op_sel_hi:[0,0,0]
	v_mfma_scale_f32_16x16x128_f8f6f4 v[142:145], v[236:243], v[192:199], v[142:145], v222, v224 op_sel_hi:[0,0,0]
	v_mfma_scale_f32_16x16x128_f8f6f4 v[134:137], v[244:251], v[192:199], v[134:137], v222, v224 op_sel_hi:[0,0,0]
	v_mfma_scale_f32_16x16x128_f8f6f4 v[126:129], v[236:243], v[228:235], v[126:129], v222, v224 op_sel_hi:[0,0,0]
	v_mfma_scale_f32_16x16x128_f8f6f4 v[118:121], v[244:251], v[228:235], v[118:121], v222, v224 op_sel_hi:[0,0,0]
	s_mov_b32 m0, s70
	v_lshl_add_u64 v[12:13], v[12:13], 0, s[22:23]
	s_barrier
	ds_read_b128 v[2:5], v221 offset:49152
	ds_read_b128 v[30:33], v221 offset:51200
	ds_read_b128 v[6:9], v227 offset:49152
	ds_read_b128 v[34:37], v227 offset:51200
	ds_read_b128 v[38:41], v221 offset:53248
	ds_read_b128 v[192:195], v221 offset:55296
	ds_read_b128 v[42:45], v227 offset:53248
	ds_read_b128 v[196:199], v227 offset:55296
	global_load_lds_dwordx4 v[12:13], off
	v_lshl_add_u64 v[12:13], v[46:47], 0, s[22:23]
	s_mov_b32 m0, s71
	s_nop 0
	global_load_lds_dwordx4 v[12:13], off
	s_barrier
	s_waitcnt lgkmcnt(0)
	s_waitcnt lgkmcnt(0)
	v_mfma_scale_f32_16x16x128_f8f6f4 v[110:113], v[14:21], v[2:9], v[110:113], v222, v224 op_sel_hi:[0,0,0]
	v_mfma_scale_f32_16x16x128_f8f6f4 v[98:101], v[22:29], v[2:9], v[98:101], v222, v224 op_sel_hi:[0,0,0]
	v_mfma_scale_f32_16x16x128_f8f6f4 v[90:93], v[14:21], v[30:37], v[90:93], v222, v224 op_sel_hi:[0,0,0]
	v_mfma_scale_f32_16x16x128_f8f6f4 v[82:85], v[22:29], v[30:37], v[82:85], v222, v224 op_sel_hi:[0,0,0]
	v_mfma_scale_f32_16x16x128_f8f6f4 v[74:77], v[14:21], v[38:45], v[74:77], v222, v224 op_sel_hi:[0,0,0]
	v_mfma_scale_f32_16x16x128_f8f6f4 v[66:69], v[22:29], v[38:45], v[66:69], v222, v224 op_sel_hi:[0,0,0]
	v_mfma_scale_f32_16x16x128_f8f6f4 v[54:57], v[14:21], v[192:199], v[54:57], v222, v224 op_sel_hi:[0,0,0]
	v_mfma_scale_f32_16x16x128_f8f6f4 v[50:53], v[22:29], v[192:199], v[50:53], v222, v224 op_sel_hi:[0,0,0]
	s_barrier
	v_lshl_add_u64 v[12:13], v[10:11], 0, s[28:29]
	s_mov_b32 m0, s72
	v_lshl_add_u64 v[14:15], v[12:13], 0, v[180:181]
	global_load_lds_dwordx4 v[14:15], off
	v_lshl_add_u64 v[12:13], v[12:13], 0, v[182:183]
	s_mov_b32 m0, s73
	s_nop 0
	global_load_lds_dwordx4 v[12:13], off
	s_waitcnt vmcnt(6)
	s_barrier
	v_mfma_scale_f32_16x16x128_f8f6f4 v[114:117], v[236:243], v[2:9], v[114:117], v222, v224 op_sel_hi:[0,0,0]
	v_mfma_scale_f32_16x16x128_f8f6f4 v[102:105], v[244:251], v[2:9], v[102:105], v222, v224 op_sel_hi:[0,0,0]
	v_mfma_scale_f32_16x16x128_f8f6f4 v[94:97], v[236:243], v[30:37], v[94:97], v222, v224 op_sel_hi:[0,0,0]
	v_mfma_scale_f32_16x16x128_f8f6f4 v[86:89], v[244:251], v[30:37], v[86:89], v222, v224 op_sel_hi:[0,0,0]
	v_mfma_scale_f32_16x16x128_f8f6f4 v[78:81], v[236:243], v[38:45], v[78:81], v222, v224 op_sel_hi:[0,0,0]
	v_mfma_scale_f32_16x16x128_f8f6f4 v[70:73], v[244:251], v[38:45], v[70:73], v222, v224 op_sel_hi:[0,0,0]
	v_mfma_scale_f32_16x16x128_f8f6f4 v[62:65], v[236:243], v[192:199], v[62:65], v222, v224 op_sel_hi:[0,0,0]
	v_mfma_scale_f32_16x16x128_f8f6f4 v[58:61], v[244:251], v[192:199], v[58:61], v222, v224 op_sel_hi:[0,0,0]
	s_and_b64 vcc, exec, s[4:5]
	s_barrier
	s_cbranch_vccz .LBB0_1448
	v_mov_b32_e32 v1, v0
	s_lshl_b32 s6, s36, 14
	s_lshl_b32 s46, s93, 2
	v_and_b32_e32 v1, 0xff, v1
	s_ashr_i32 s39, s38, 31
	s_ashr_i32 s7, s6, 31
	s_add_i32 s47, s77, s46
	s_lshl_b64 s[44:45], s[36:37], 14
	s_add_i32 m0, s76, s46
	v_add_u32_e32 v2, 0x780, v1
	v_cmp_gt_u32_e32 vcc, s66, v1
	s_add_u32 s44, s81, s44
	s_addc_u32 s45, s82, s45
	v_cndmask_b32_e32 v1, v2, v1, vcc
	v_lshlrev_b32_e32 v1, 2, v1
	s_lshl_b64 s[6:7], s[6:7], 2
	global_load_lds_dword v1, s[44:45]
	s_add_u32 s44, s20, s6
	v_mov_b32_e32 v1, v0
	s_addc_u32 s45, s21, s7
	s_lshl_b64 s[6:7], s[38:39], 2
	s_add_u32 s6, s44, s6
	s_addc_u32 s7, s45, s7
	v_lshlrev_b32_sdwa v1, v225, v1 dst_sel:DWORD dst_unused:UNUSED_PAD src0_sel:DWORD src1_sel:BYTE_0
	s_mov_b32 m0, s47
	s_nop 0
	global_load_lds_dword v1, s[6:7]

; #define LAS __attribute__((address_space(3)))
; #define G_GATHER_OFFS(tab_, rv_) do { _Pragma("unroll") for (int i = 0; i < 2; ++i) { int R_, C_; G_SRC(i, R_, C_); const int ra_ = (tab_)[R_], rb_ = (tab_)[HALF + R_];        \
;     vAc[0][i] = (unsigned)((R_ < (rv_) ? ra_ : 0) * KB + C_); vAc[1][i] = (unsigned)((HALF + R_ < (rv_) ? rb_ : 0) * KB + C_); } } while (0)
; #define G_STAGE(bufoff, gbase, voff) do { _Pragma("unroll") for (int _i = 0; _i < 2; ++_i) \
;     __builtin_amdgcn_global_load_lds((const unsigned*)((const char*)(gbase) + (voff)[_i]), (LAS unsigned*)(lds + (bufoff) + ldsw + _i * 8192), 16, 0, 0); } while (0)
; #define G_LDA(dst, b, h) do { _Pragma("unroll") for (int m = 0; m < 4; ++m) dst[m] = G_LD2(G_SA(b, h) + aoff + m * 2048, G_SA(b, h) + (P::FP8 ? aoff1 : aoff + 1024) + m * 2048); } while (0)
; #define G_LDB(dst, b, h) do { _Pragma("unroll") for (int n = 0; n < 2; ++n) dst[n] = G_LD2(G_SB(b, h) + boff + n * 2048, G_SB(b, h) + (P::FP8 ? boff1 : boff + 1024) + n * 2048); } while (0)
; #define BAR __builtin_amdgcn_s_barrier()
; template <class P>
; DEV void gemm_stream(const P& pol) {
;     ...
;     for (int t = 0; t < nt; t += 2) {
;       const bool last = (t == nt - 2);
;       const size_t k1 = (size_t)(t + 1) * kstep, k2 = (size_t)(t + 2) * kstep;
;       const char* a20 = last ? nA0 : cA0 + k2; const char* a21 = last ? nA1 : cA1 + k2; const char* b2 = last ? nB : cB + k2;
;       G_LDB(B0, 0, 0); SCHED; G_LDA(At, 0, 0); G_STAGE(G_SA(1, 1), cA1 + k1, vAc[1]);
;       WAIT_L(8); BAR; WAIT_L(0); G_MMA(0, 0, At, B0); BAR; SCHED;
;       if (P::GATHER && last && has_next) { LAS int* tab = arow + ((ui + 1) & 1) * 256; G_GATHER_OFFS(tab, nxt.rv); }
;       G_LDB(B1, 0, 1); G_STAGE(G_SB(0, 0), b2, voffB);
;       BAR; WAIT_L(0); G_MMA(0, 1, At, B1); BAR;
;       G_LDA(At, 0, 1); G_STAGE(G_SA(0, 0), a20, vAc[0]);
;       BAR; WAIT_L(0); G_MMA(1, 0, At, B0); BAR; SCHED;
;       G_STAGE(G_SB(0, 1), b2 + hstep, voffB);
;       WAIT_V(6); BAR; G_MMA(1, 1, At, B1); BAR;
;       G_LDB(B0, 1, 0); SCHED; G_LDA(At, 1, 0); G_STAGE(G_SA(0, 1), a21, vAc[1]);
;       WAIT_L(8); BAR; WAIT_L(0); G_MMA(0, 0, At, B0); BAR; SCHED;
;       G_LDB(B1, 1, 1); G_STAGE(G_SB(1, 0), b2 + kstep, voffB);
;       BAR; WAIT_L(0); G_MMA(0, 1, At, B1); BAR;
;       G_LDA(At, 1, 1); G_STAGE(G_SA(1, 0), a20 + kstep, vAc[0]);
;       BAR; WAIT_L(0); G_MMA(1, 0, At, B0); BAR; SCHED;
.LBB0_1450:
	v_lshl_add_u64 v[194:195], v[192:193], 0, s[46:47]
	v_cndmask_b32_e64 v195, v195, v1, s[6:7]
	v_cndmask_b32_e64 v194, v194, v190, s[6:7]
	s_mov_b32 m0, s59
	v_lshl_add_u64 v[196:197], v[194:195], 0, v[180:181]
	ds_read_b128 v[228:231], v212
	ds_read_b128 v[232:235], v206
	ds_read_b128 v[236:239], v213
	ds_read_b128 v[240:243], v214
	global_load_lds_dwordx4 v[196:197], off
	v_lshl_add_u64 v[198:199], v[194:195], 0, v[182:183]
	s_mov_b32 m0, s60
	s_add_u32 s95, s46, 0x200
	global_load_lds_dwordx4 v[198:199], off
	s_addc_u32 s96, s47, 0
	s_and_b64 s[6:7], s[6:7], exec
	s_barrier
	s_waitcnt lgkmcnt(0)
	s_cselect_b32 s6, 0, s95
	s_cselect_b32 s7, 0, s96
	s_add_u32 s6, s10, s6
	s_addc_u32 s7, s11, s7
	s_waitcnt lgkmcnt(0)
	v_mfma_scale_f32_16x16x128_f8f6f4 v[174:177], v[228:235], v[18:25], v[174:177], v222, v224 op_sel_hi:[0,0,0]
	v_mfma_scale_f32_16x16x128_f8f6f4 v[166:169], v[236:243], v[18:25], v[166:169], v222, v224 op_sel_hi:[0,0,0]
	v_mfma_scale_f32_16x16x128_f8f6f4 v[158:161], v[228:235], v[26:33], v[158:161], v222, v224 op_sel_hi:[0,0,0]
	v_mfma_scale_f32_16x16x128_f8f6f4 v[150:153], v[236:243], v[26:33], v[150:153], v222, v224 op_sel_hi:[0,0,0]
	v_mfma_scale_f32_16x16x128_f8f6f4 v[142:145], v[228:235], v[34:41], v[142:145], v222, v224 op_sel_hi:[0,0,0]
	v_mfma_scale_f32_16x16x128_f8f6f4 v[134:137], v[236:243], v[34:41], v[134:137], v222, v224 op_sel_hi:[0,0,0]
	v_mfma_scale_f32_16x16x128_f8f6f4 v[126:129], v[228:235], v[42:49], v[126:129], v222, v224 op_sel_hi:[0,0,0]
	v_mfma_scale_f32_16x16x128_f8f6f4 v[118:121], v[236:243], v[42:49], v[118:121], v222, v224 op_sel_hi:[0,0,0]
	s_mov_b32 m0, s58
	s_barrier
	ds_read_b128 v[22:25], v221 offset:16384
	ds_read_b128 v[30:33], v221 offset:18432
	ds_read_b128 v[26:29], v227 offset:16384
	ds_read_b128 v[34:37], v227 offset:18432
	ds_read_b128 v[38:41], v221 offset:20480
	ds_read_b128 v[244:247], v221 offset:22528
	ds_read_b128 v[42:45], v227 offset:20480
	ds_read_b128 v[248:251], v227 offset:22528
	global_load_lds_dwordx4 v178, s[6:7]
	s_mov_b32 m0, s61
	v_mov_b32_e32 v185, v179
	global_load_lds_dwordx4 v184, s[6:7]
	s_barrier
	s_waitcnt lgkmcnt(0)
	v_lshl_add_u64 v[20:21], s[6:7], 0, v[178:179]
	v_lshl_add_u64 v[18:19], s[6:7], 0, v[184:185]
	s_waitcnt lgkmcnt(0)
	v_mfma_scale_f32_16x16x128_f8f6f4 v[110:113], v[2:9], v[22:29], v[110:113], v222, v224 op_sel_hi:[0,0,0]
	v_mfma_scale_f32_16x16x128_f8f6f4 v[98:101], v[10:17], v[22:29], v[98:101], v222, v224 op_sel_hi:[0,0,0]
	v_mfma_scale_f32_16x16x128_f8f6f4 v[90:93], v[2:9], v[30:37], v[90:93], v222, v224 op_sel_hi:[0,0,0]
	v_mfma_scale_f32_16x16x128_f8f6f4 v[82:85], v[10:17], v[30:37], v[82:85], v222, v224 op_sel_hi:[0,0,0]
	v_mfma_scale_f32_16x16x128_f8f6f4 v[74:77], v[2:9], v[38:45], v[74:77], v222, v224 op_sel_hi:[0,0,0]
	v_mfma_scale_f32_16x16x128_f8f6f4 v[66:69], v[10:17], v[38:45], v[66:69], v222, v224 op_sel_hi:[0,0,0]
	v_mfma_scale_f32_16x16x128_f8f6f4 v[54:57], v[2:9], v[244:251], v[54:57], v222, v224 op_sel_hi:[0,0,0]
	v_mfma_scale_f32_16x16x128_f8f6f4 v[50:53], v[10:17], v[244:251], v[50:53], v222, v224 op_sel_hi:[0,0,0]
	s_barrier
	v_lshl_add_u64 v[2:3], v[194:195], 0, s[12:13]
	s_mov_b32 m0, s62
	v_lshl_add_u64 v[4:5], v[2:3], 0, v[180:181]
	global_load_lds_dwordx4 v[4:5], off
	v_lshl_add_u64 v[2:3], v[2:3], 0, v[182:183]
	s_mov_b32 m0, s63
	s_nop 0
	global_load_lds_dwordx4 v[2:3], off
	s_waitcnt vmcnt(6)
	s_barrier
	v_mfma_scale_f32_16x16x128_f8f6f4 v[114:117], v[228:235], v[22:29], v[114:117], v222, v224 op_sel_hi:[0,0,0]
	v_mfma_scale_f32_16x16x128_f8f6f4 v[102:105], v[236:243], v[22:29], v[102:105], v222, v224 op_sel_hi:[0,0,0]
	v_mfma_scale_f32_16x16x128_f8f6f4 v[94:97], v[228:235], v[30:37], v[94:97], v222, v224 op_sel_hi:[0,0,0]
	v_mfma_scale_f32_16x16x128_f8f6f4 v[86:89], v[236:243], v[30:37], v[86:89], v222, v224 op_sel_hi:[0,0,0]
	v_mfma_scale_f32_16x16x128_f8f6f4 v[78:81], v[228:235], v[38:45], v[78:81], v222, v224 op_sel_hi:[0,0,0]
	v_mfma_scale_f32_16x16x128_f8f6f4 v[70:73], v[236:243], v[38:45], v[70:73], v222, v224 op_sel_hi:[0,0,0]
	v_mfma_scale_f32_16x16x128_f8f6f4 v[62:65], v[228:235], v[244:251], v[62:65], v222, v224 op_sel_hi:[0,0,0]
	v_mfma_scale_f32_16x16x128_f8f6f4 v[58:61], v[236:243], v[244:251], v[58:61], v222, v224 op_sel_hi:[0,0,0]
	s_barrier
	ds_read_b128 v[2:5], v215
	ds_read_b128 v[6:9], v207
	ds_read_b128 v[10:13], v216
	ds_read_b128 v[14:17], v217
	s_mov_b32 m0, s64
	v_lshl_add_u64 v[46:47], s[6:7], 0, v[200:201]
	ds_read_b128 v[22:25], v221 offset:32768
	ds_read_b128 v[30:33], v221 offset:34816
	ds_read_b128 v[26:29], v227 offset:32768
	ds_read_b128 v[34:37], v227 offset:34816
	ds_read_b128 v[38:41], v221 offset:36864
	ds_read_b128 v[228:231], v221 offset:38912
	ds_read_b128 v[42:45], v227 offset:36864
	ds_read_b128 v[232:235], v227 offset:38912
	global_load_lds_dwordx4 v[46:47], off
	v_lshl_add_u64 v[46:47], s[6:7], 0, v[188:189]
	s_mov_b32 m0, s65
	s_nop 0
	global_load_lds_dwordx4 v[46:47], off
	s_waitcnt lgkmcnt(8)
	s_barrier
	s_waitcnt lgkmcnt(0)
	s_waitcnt lgkmcnt(0)
	v_mfma_scale_f32_16x16x128_f8f6f4 v[170:173], v[2:9], v[22:29], v[170:173], v222, v224 op_sel_hi:[0,0,0]
	v_mfma_scale_f32_16x16x128_f8f6f4 v[162:165], v[10:17], v[22:29], v[162:165], v222, v224 op_sel_hi:[0,0,0]
	v_mfma_scale_f32_16x16x128_f8f6f4 v[154:157], v[2:9], v[30:37], v[154:157], v222, v224 op_sel_hi:[0,0,0]
	v_mfma_scale_f32_16x16x128_f8f6f4 v[146:149], v[10:17], v[30:37], v[146:149], v222, v224 op_sel_hi:[0,0,0]
	v_mfma_scale_f32_16x16x128_f8f6f4 v[138:141], v[2:9], v[38:45], v[138:141], v222, v224 op_sel_hi:[0,0,0]
	v_mfma_scale_f32_16x16x128_f8f6f4 v[130:133], v[10:17], v[38:45], v[130:133], v222, v224 op_sel_hi:[0,0,0]
	v_mfma_scale_f32_16x16x128_f8f6f4 v[122:125], v[2:9], v[228:235], v[122:125], v222, v224 op_sel_hi:[0,0,0]
	v_mfma_scale_f32_16x16x128_f8f6f4 v[106:109], v[10:17], v[228:235], v[106:109], v222, v224 op_sel_hi:[0,0,0]
	s_barrier
; #define LAS __attribute__((address_space(3)))
; #define G_GATHER_OFFS(tab_, rv_) do { _Pragma("unroll") for (int i = 0; i < 2; ++i) { int R_, C_; G_SRC(i, R_, C_); const int ra_ = (tab_)[R_], rb_ = (tab_)[HALF + R_];        \
;     vAc[0][i] = (unsigned)((R_ < (rv_) ? ra_ : 0) * KB + C_); vAc[1][i] = (unsigned)((HALF + R_ < (rv_) ? rb_ : 0) * KB + C_); } } while (0)
; #define G_STAGE(bufoff, gbase, voff) do { _Pragma("unroll") for (int _i = 0; _i < 2; ++_i) \
;     __builtin_amdgcn_global_load_lds((const unsigned*)((const char*)(gbase) + (voff)[_i]), (LAS unsigned*)(lds + (bufoff) + ldsw + _i * 8192), 16, 0, 0); } while (0)
; #define WAIT_V(n) asm volatile("s_waitcnt vmcnt(" #n ")" ::: "memory")
; template <class P>
; DEV void gemm_stream(const P& pol) {
;     ...
;     for (int t = 0; t < nt; t += 2) {
;       const bool last = (t == nt - 2);
;       const size_t k1 = (size_t)(t + 1) * kstep, k2 = (size_t)(t + 2) * kstep;
;       const char* a20 = last ? nA0 : cA0 + k2; const char* a21 = last ? nA1 : cA1 + k2; const char* b2 = last ? nB : cB + k2;
;       G_LDB(B0, 0, 0); SCHED; G_LDA(At, 0, 0); G_STAGE(G_SA(1, 1), cA1 + k1, vAc[1]);
;       WAIT_L(8); BAR; WAIT_L(0); G_MMA(0, 0, At, B0); BAR; SCHED;
;       if (P::GATHER && last && has_next) { LAS int* tab = arow + ((ui + 1) & 1) * 256; G_GATHER_OFFS(tab, nxt.rv); }
;       G_LDB(B1, 0, 1); G_STAGE(G_SB(0, 0), b2, voffB);
;       BAR; WAIT_L(0); G_MMA(0, 1, At, B1); BAR;
;       G_LDA(At, 0, 1); G_STAGE(G_SA(0, 0), a20, vAc[0]);
;       BAR; WAIT_L(0); G_MMA(1, 0, At, B0); BAR; SCHED;
;       G_STAGE(G_SB(0, 1), b2 + hstep, voffB);
;       WAIT_V(6); BAR; G_MMA(1, 1, At, B1); BAR;
;       G_LDB(B0, 1, 0); SCHED; G_LDA(At, 1, 0); G_STAGE(G_SA(0, 1), a21, vAc[1]);
;       WAIT_L(8); BAR; WAIT_L(0); G_MMA(0, 0, At, B0); BAR; SCHED;
;       G_LDB(B1, 1, 1); G_STAGE(G_SB(1, 0), b2 + kstep, voffB);
;       BAR; WAIT_L(0); G_MMA(0, 1, At, B1); BAR;
;       G_LDA(At, 1, 1); G_STAGE(G_SA(1, 0), a20 + kstep, vAc[0]);
;       BAR; WAIT_L(0); G_MMA(1, 0, At, B0); BAR; SCHED;
;       G_STAGE(G_SB(1, 1), b2 + hstep + kstep, voffB);
;       WAIT_V(6); BAR; G_MMA(1, 1, At, B1); BAR;
;       if (P::HASBIAS && has_next && t == 0) pol.bias_dma(nxt, btab + ((ui + 1) & 1) * 256 + ((wid & 3) << 6));
;       if (P::GATHER && has_next && t == 0) pol.arow_dma(nxt, arow + ((ui + 1) & 1) * 256 + ((wid & 3) << 6));
;     }
	s_mov_b32 m0, s68
	v_lshl_add_u64 v[46:47], v[196:197], 0, s[14:15]
	ds_read_b128 v[236:239], v218
	ds_read_b128 v[240:243], v208
	ds_read_b128 v[244:247], v219
	ds_read_b128 v[248:251], v220
	global_load_lds_dwordx4 v[46:47], off
	v_lshl_add_u64 v[46:47], v[198:199], 0, s[14:15]
	s_mov_b32 m0, s69
	s_nop 0
	global_load_lds_dwordx4 v[46:47], off
	s_barrier
	s_waitcnt lgkmcnt(0)
	s_waitcnt lgkmcnt(0)
	v_mfma_scale_f32_16x16x128_f8f6f4 v[174:177], v[236:243], v[22:29], v[174:177], v222, v224 op_sel_hi:[0,0,0]
	v_mfma_scale_f32_16x16x128_f8f6f4 v[166:169], v[244:251], v[22:29], v[166:169], v222, v224 op_sel_hi:[0,0,0]
	v_mfma_scale_f32_16x16x128_f8f6f4 v[158:161], v[236:243], v[30:37], v[158:161], v222, v224 op_sel_hi:[0,0,0]
	v_mfma_scale_f32_16x16x128_f8f6f4 v[150:153], v[244:251], v[30:37], v[150:153], v222, v224 op_sel_hi:[0,0,0]
	v_mfma_scale_f32_16x16x128_f8f6f4 v[142:145], v[236:243], v[38:45], v[142:145], v222, v224 op_sel_hi:[0,0,0]
	v_mfma_scale_f32_16x16x128_f8f6f4 v[134:137], v[244:251], v[38:45], v[134:137], v222, v224 op_sel_hi:[0,0,0]
	v_mfma_scale_f32_16x16x128_f8f6f4 v[126:129], v[236:243], v[228:235], v[126:129], v222, v224 op_sel_hi:[0,0,0]
	v_mfma_scale_f32_16x16x128_f8f6f4 v[118:121], v[244:251], v[228:235], v[118:121], v222, v224 op_sel_hi:[0,0,0]
	s_mov_b32 m0, s70
	v_lshl_add_u64 v[20:21], v[20:21], 0, s[14:15]
	s_barrier
	ds_read_b128 v[22:25], v221 offset:49152
	ds_read_b128 v[30:33], v221 offset:51200
	ds_read_b128 v[26:29], v227 offset:49152
	ds_read_b128 v[34:37], v227 offset:51200
	ds_read_b128 v[38:41], v221 offset:53248
	ds_read_b128 v[228:231], v221 offset:55296
	ds_read_b128 v[42:45], v227 offset:53248
	ds_read_b128 v[232:235], v227 offset:55296
	global_load_lds_dwordx4 v[20:21], off
	v_lshl_add_u64 v[18:19], v[18:19], 0, s[14:15]
	s_mov_b32 m0, s71
	s_nop 0
	global_load_lds_dwordx4 v[18:19], off
	s_barrier
	s_waitcnt lgkmcnt(0)
	s_waitcnt lgkmcnt(0)
	v_mfma_scale_f32_16x16x128_f8f6f4 v[110:113], v[2:9], v[22:29], v[110:113], v222, v224 op_sel_hi:[0,0,0]
	v_mfma_scale_f32_16x16x128_f8f6f4 v[98:101], v[10:17], v[22:29], v[98:101], v222, v224 op_sel_hi:[0,0,0]
	v_mfma_scale_f32_16x16x128_f8f6f4 v[90:93], v[2:9], v[30:37], v[90:93], v222, v224 op_sel_hi:[0,0,0]
	v_mfma_scale_f32_16x16x128_f8f6f4 v[82:85], v[10:17], v[30:37], v[82:85], v222, v224 op_sel_hi:[0,0,0]
	v_mfma_scale_f32_16x16x128_f8f6f4 v[74:77], v[2:9], v[38:45], v[74:77], v222, v224 op_sel_hi:[0,0,0]
	v_mfma_scale_f32_16x16x128_f8f6f4 v[66:69], v[10:17], v[38:45], v[66:69], v222, v224 op_sel_hi:[0,0,0]
	v_mfma_scale_f32_16x16x128_f8f6f4 v[54:57], v[2:9], v[228:235], v[54:57], v222, v224 op_sel_hi:[0,0,0]
	v_mfma_scale_f32_16x16x128_f8f6f4 v[50:53], v[10:17], v[228:235], v[50:53], v222, v224 op_sel_hi:[0,0,0]
	s_barrier
	v_lshl_add_u64 v[2:3], v[194:195], 0, s[16:17]
	s_mov_b32 m0, s72
	v_lshl_add_u64 v[4:5], v[2:3], 0, v[180:181]
	global_load_lds_dwordx4 v[4:5], off
	v_lshl_add_u64 v[2:3], v[2:3], 0, v[182:183]
	s_mov_b32 m0, s73
	s_nop 0
	global_load_lds_dwordx4 v[2:3], off
	s_waitcnt vmcnt(6)
	s_barrier
	v_mfma_scale_f32_16x16x128_f8f6f4 v[114:117], v[236:243], v[22:29], v[114:117], v222, v224 op_sel_hi:[0,0,0]
	v_mfma_scale_f32_16x16x128_f8f6f4 v[102:105], v[244:251], v[22:29], v[102:105], v222, v224 op_sel_hi:[0,0,0]
	v_mfma_scale_f32_16x16x128_f8f6f4 v[94:97], v[236:243], v[30:37], v[94:97], v222, v224 op_sel_hi:[0,0,0]
	v_mfma_scale_f32_16x16x128_f8f6f4 v[86:89], v[244:251], v[30:37], v[86:89], v222, v224 op_sel_hi:[0,0,0]
	v_mfma_scale_f32_16x16x128_f8f6f4 v[78:81], v[236:243], v[38:45], v[78:81], v222, v224 op_sel_hi:[0,0,0]
	v_mfma_scale_f32_16x16x128_f8f6f4 v[70:73], v[244:251], v[38:45], v[70:73], v222, v224 op_sel_hi:[0,0,0]
	v_mfma_scale_f32_16x16x128_f8f6f4 v[62:65], v[236:243], v[228:235], v[62:65], v222, v224 op_sel_hi:[0,0,0]
	v_mfma_scale_f32_16x16x128_f8f6f4 v[58:61], v[244:251], v[228:235], v[58:61], v222, v224 op_sel_hi:[0,0,0]
	s_add_i32 s39, s39, 2
	s_add_u32 s46, s46, 0x100
	s_addc_u32 s47, s47, 0
	s_cmp_gt_u32 s39, 13
	s_barrier
	s_cbranch_scc1 .LBB0_1453
.LBB0_1451:
	ds_read_b128 v[2:5], v209
	ds_read_b128 v[6:9], v205
	ds_read_b128 v[10:13], v210
	ds_read_b128 v[14:17], v211
	s_cmp_eq_u32 s39, 12
	s_cselect_b64 s[6:7], -1, 0
	s_add_u32 s96, s83, s46
	s_addc_u32 s97, s84, s47
	s_mov_b32 m0, s85
	ds_read_b128 v[18:21], v221
	ds_read_b128 v[26:29], v221 offset:2048
	ds_read_b128 v[22:25], v227
	ds_read_b128 v[30:33], v227 offset:2048
	ds_read_b128 v[34:37], v221 offset:4096
	ds_read_b128 v[42:45], v221 offset:6144
	ds_read_b128 v[38:41], v227 offset:4096
	ds_read_b128 v[46:49], v227 offset:6144
	global_load_lds_dwordx4 v186, s[96:97]
	s_mov_b32 m0, s86
	s_nop 0
	global_load_lds_dwordx4 v188, s[96:97]
	s_waitcnt lgkmcnt(8)
	s_barrier
	s_waitcnt lgkmcnt(0)
	s_waitcnt lgkmcnt(0)
	v_mfma_scale_f32_16x16x128_f8f6f4 v[170:173], v[2:9], v[18:25], v[170:173], v222, v224 op_sel_hi:[0,0,0]
	v_mfma_scale_f32_16x16x128_f8f6f4 v[162:165], v[10:17], v[18:25], v[162:165], v222, v224 op_sel_hi:[0,0,0]
	v_mfma_scale_f32_16x16x128_f8f6f4 v[154:157], v[2:9], v[26:33], v[154:157], v222, v224 op_sel_hi:[0,0,0]
	v_mfma_scale_f32_16x16x128_f8f6f4 v[146:149], v[10:17], v[26:33], v[146:149], v222, v224 op_sel_hi:[0,0,0]
	v_mfma_scale_f32_16x16x128_f8f6f4 v[138:141], v[2:9], v[34:41], v[138:141], v222, v224 op_sel_hi:[0,0,0]
	v_mfma_scale_f32_16x16x128_f8f6f4 v[130:133], v[10:17], v[34:41], v[130:133], v222, v224 op_sel_hi:[0,0,0]
	v_mfma_scale_f32_16x16x128_f8f6f4 v[122:125], v[2:9], v[42:49], v[122:125], v222, v224 op_sel_hi:[0,0,0]
	v_mfma_scale_f32_16x16x128_f8f6f4 v[106:109], v[10:17], v[42:49], v[106:109], v222, v224 op_sel_hi:[0,0,0]
	s_barrier
	s_and_b64 s[96:97], s[4:5], s[6:7]
	s_andn2_b64 vcc, exec, s[96:97]
	s_cbranch_vccz .LBB0_1449
	v_mov_b32_e32 v187, v179
	v_mov_b32_e32 v189, v179
	v_mov_b64_e32 v[200:201], v[186:187]
	s_branch .LBB0_1450

; #define WAIT_V(n) asm volatile("s_waitcnt vmcnt(" #n ")" ::: "memory")
; #define BAR __builtin_amdgcn_s_barrier()
; template <class P>
; DEV void gemm_stream(const P& pol) {
;     ...
;   WAIT_V(0);
;   if (wr == 0) BAR;
;   __syncthreads();
.LBB0_1455:
	s_setprio 0
	s_waitcnt vmcnt(0)
	s_cmpk_gt_u32 s54, 0xff
	s_cbranch_scc1 .LBB0_1457
	s_barrier
